# dilated units: previous unit's epilogue deferred until after this unit's tile DMAs are issued
# speedup vs baseline: 1.0307x; 1.0002x over previous
; __device__ __forceinline__ unsigned cvtpk(float lo, float hi) { f32x2_t v = {lo, hi}; bf16x2_t b = __builtin_convertvector(v, bf16x2_t); return __builtin_bit_cast(unsigned, b); }
; __device__ __forceinline__ int crow(int r, int hi) { return (r & 3) + 8 * (r >> 2) + 4 * hi; }
; template <class BIAS>
; __device__ __forceinline__ void attn_tiles(char* shm, const UnitIO& io, int t_begin, int t_end, const BIAS& B, int tid) {
;     ...
;     { bf16* stg = (bf16*)(shm + LDS_OST) + wid * 2048;
; #pragma unroll
;       for (int r = 0; r < 16; ++r) { const int orow = crow(r, hi);
; #pragma unroll
;           for (int d0 = 0; d0 < 2; ++d0) stg[orow * 64 + d0 * 32 + r32] = (bf16)(cvtpk(o[d0][r] * rli[r], 0.f) & 0xffffu); }
;       asm volatile("s_waitcnt lgkmcnt(0)" ::: "memory");
; #pragma unroll
;       for (int i = 0; i < 4; ++i) { const int row = i * 8 + (lane >> 3), ch = lane & 7; const u32x4 v = *(const u32x4*)(stg + row * 64 + ch * 8); __builtin_nontemporal_store(v, (u32x4*)(io.O + (long)row * io.ostride + ch * 8)); } }
; __device__ __forceinline__ void dil_unit(Frame& F, const AttnBufs& A, int b, int h, int g, int r, int c) {
;     ...
;     const int dil = (g == 0) ? 1 : (g == 1 ? 4 : 16);
;     const int i0 = 256 * c;
;     att::BiasDil B; B.sd = exp2f(-8.0f * (float)(h - 10 + 1) / 10.0f) * LOG2E * (float)dil; B.qrel = 128 + w * 32 + r32; B.hi = hi; B.w = w; B.setup(r32);
.LBB0_362:
	s_or_b64 exec, exec, s[56:57]
	s_and_b64 s[56:57], s[64:65], exec
	s_movk_i32 s56, 0x1800
	v_readlane_b32 s2, v190, 7
	s_cselect_b32 s64, 0x600, s56
	s_mul_hi_u32 s56, s2, 0x1800000
	s_mul_i32 s57, s2, 0x1800000
	v_readlane_b32 s2, v255, 23
	s_add_u32 s57, s2, s57
	v_readlane_b32 s2, v255, 24
	s_mul_i32 s65, s67, 0x300
	s_mul_hi_u32 s67, s66, 0x300
	s_addc_u32 s56, s2, s56
	s_add_i32 s67, s67, s65
	s_mul_i32 s65, s66, 0x300
	s_add_u32 s57, s57, s65
	v_readlane_b32 s2, v190, 9
	s_addc_u32 s65, s56, s67
	s_lshl_b32 s56, s2, 1
	s_add_u32 s56, s57, s56
	s_addc_u32 s57, s65, 0
	s_lshl_b32 s65, s76, 12
	s_add_i32 s65, s65, 0x10800
	v_cvt_pk_bf16_f32 v0, v2, s0
	v_lshl_or_b32 v2, v179, 1, s65
	v_lshl_add_u32 v2, v146, 1, v2
	ds_write_b16 v2, v0
	v_cvt_pk_bf16_f32 v0, v18, s0
	ds_write_b16 v2, v0 offset:64
	v_cvt_pk_bf16_f32 v0, v3, s0
	ds_write_b16 v2, v0 offset:128
	v_cvt_pk_bf16_f32 v0, v19, s0
	ds_write_b16 v2, v0 offset:192
	v_cvt_pk_bf16_f32 v0, v4, s0
	ds_write_b16 v2, v0 offset:256
	v_cvt_pk_bf16_f32 v0, v20, s0
	ds_write_b16 v2, v0 offset:320
	v_cvt_pk_bf16_f32 v0, v5, s0
	ds_write_b16 v2, v0 offset:384
	v_cvt_pk_bf16_f32 v0, v21, s0
	ds_write_b16 v2, v0 offset:448
	v_cvt_pk_bf16_f32 v0, v6, s0
	ds_write_b16 v2, v0 offset:1024
	v_cvt_pk_bf16_f32 v0, v22, s0
	ds_write_b16 v2, v0 offset:1088
	v_cvt_pk_bf16_f32 v0, v7, s0
	ds_write_b16 v2, v0 offset:1152
	v_cvt_pk_bf16_f32 v0, v23, s0
	ds_write_b16 v2, v0 offset:1216
	v_cvt_pk_bf16_f32 v0, v8, s0
	ds_write_b16 v2, v0 offset:1280
	v_cvt_pk_bf16_f32 v0, v24, s0
	ds_write_b16 v2, v0 offset:1344
	v_cvt_pk_bf16_f32 v0, v9, s0
	ds_write_b16 v2, v0 offset:1408
	v_cvt_pk_bf16_f32 v0, v25, s0
	ds_write_b16 v2, v0 offset:1472
	v_cvt_pk_bf16_f32 v0, v10, s0
	ds_write_b16 v2, v0 offset:2048
	v_cvt_pk_bf16_f32 v0, v26, s0
	ds_write_b16 v2, v0 offset:2112
	v_cvt_pk_bf16_f32 v0, v11, s0
	ds_write_b16 v2, v0 offset:2176
	v_cvt_pk_bf16_f32 v0, v27, s0
	ds_write_b16 v2, v0 offset:2240
	v_cvt_pk_bf16_f32 v0, v12, s0
	ds_write_b16 v2, v0 offset:2304
	v_cvt_pk_bf16_f32 v0, v28, s0
	ds_write_b16 v2, v0 offset:2368
	v_cvt_pk_bf16_f32 v0, v13, s0
	ds_write_b16 v2, v0 offset:2432
	v_cvt_pk_bf16_f32 v0, v29, s0
	ds_write_b16 v2, v0 offset:2496
	v_cvt_pk_bf16_f32 v0, v14, s0
	ds_write_b16 v2, v0 offset:3072
	v_cvt_pk_bf16_f32 v0, v30, s0
	ds_write_b16 v2, v0 offset:3136
	v_cvt_pk_bf16_f32 v0, v15, s0
	ds_write_b16 v2, v0 offset:3200
	v_cvt_pk_bf16_f32 v0, v31, s0
	ds_write_b16 v2, v0 offset:3264
	v_cvt_pk_bf16_f32 v0, v16, s0
	ds_write_b16 v2, v0 offset:3328
	v_cvt_pk_bf16_f32 v0, v32, s0
	ds_write_b16 v2, v0 offset:3392
	v_cvt_pk_bf16_f32 v0, v17, s0
	ds_write_b16 v2, v0 offset:3456
	v_cvt_pk_bf16_f32 v0, v33, s0
	ds_write_b16 v2, v0 offset:3520
	v_or_b32_e32 v8, s65, v152
	s_waitcnt lgkmcnt(0)
	v_add_u32_e32 v0, v8, v183
	s_and_b64 s[62:63], s[62:63], exec
	ds_read_b128 v[2:5], v0
	s_cselect_b32 s62, 0x180, s64
	v_mul_u32_u24_e32 v0, s62, v182
	v_lshlrev_b32_e32 v0, 1, v0
	v_lshl_add_u64 v[6:7], s[56:57], 0, v[0:1]
	v_mov_b32_e32 v153, v1
	v_lshl_add_u64 v[6:7], v[6:7], 0, v[152:153]
	s_waitcnt lgkmcnt(0)
	global_store_dwordx4 v[6:7], v[2:5], off nt
	v_add_u32_e32 v0, v8, v185
	ds_read_b128 v[2:5], v0
	v_mul_u32_u24_e32 v0, s62, v184
	v_lshlrev_b32_e32 v0, 1, v0
	v_lshl_add_u64 v[6:7], s[56:57], 0, v[0:1]
	v_lshl_add_u64 v[6:7], v[6:7], 0, v[152:153]
	s_waitcnt lgkmcnt(0)
	global_store_dwordx4 v[6:7], v[2:5], off nt
	v_add_u32_e32 v0, v8, v187
	ds_read_b128 v[2:5], v0
	v_mul_u32_u24_e32 v0, s62, v186
	v_lshlrev_b32_e32 v0, 1, v0
	v_lshl_add_u64 v[6:7], s[56:57], 0, v[0:1]
	v_lshl_add_u64 v[6:7], v[6:7], 0, v[152:153]
	s_waitcnt lgkmcnt(0)
	global_store_dwordx4 v[6:7], v[2:5], off nt
	v_add_u32_e32 v0, v8, v189
	ds_read_b128 v[2:5], v0
	v_mul_u32_u24_e32 v0, s62, v188
	v_lshlrev_b32_e32 v0, 1, v0
	v_lshl_add_u64 v[6:7], s[56:57], 0, v[0:1]
	v_lshl_add_u64 v[6:7], v[6:7], 0, v[152:153]
	s_waitcnt lgkmcnt(0)
	global_store_dwordx4 v[6:7], v[2:5], off nt
	s_waitcnt lgkmcnt(0)
	v_readlane_b32 s3, v254, 10
	s_cmp_eq_u32 s100, 0
	s_cbranch_scc1 .Ldl_ret
	s_branch .LBB0_393
.LBB0_363:
	v_mov_b32_e32 v59, v1
	s_lshl_b32 s56, s74, 5
	v_readlane_b32 s2, v254, 30
	s_or_b32 s56, s56, s2
	s_mul_hi_u32 s57, s56, 0xaaaaaaab
	s_lshr_b32 s75, s57, 5
	s_mul_i32 s57, s75, 48
	s_sub_i32 s66, s56, s57
	s_lshr_b32 s2, s66, 4
	s_and_b32 s67, s66, 15
	s_cmp_lt_u32 s66, 16
	s_cselect_b64 s[62:63], -1, 0
	s_cmp_eq_u32 s2, 1
	s_cselect_b64 s[64:65], -1, 0
	s_bfe_u32 s68, s66, 0x20002
	s_and_b64 s[56:57], s[64:65], exec
	s_cselect_b32 s68, s68, s67
	s_and_b64 s[56:57], s[62:63], exec
	s_cselect_b32 s68, 0, s68
	s_and_b32 s66, s66, 3
	s_and_b64 s[56:57], s[64:65], exec
	s_cselect_b32 s66, s66, 0
	s_and_b64 s[56:57], s[62:63], exec
	s_cselect_b32 s76, s67, s66
	s_and_b64 s[56:57], s[64:65], exec
	s_cselect_b32 s66, 4, 16
	s_and_b64 s[56:57], s[62:63], exec
	s_cselect_b32 s80, 1, s66
	s_not_b32 s56, s75
	s_lshl_b32 s56, s56, 3
	v_cvt_f32_i32_e32 v58, s56
	s_mov_b32 s84, 0x41200000
	s_mov_b32 s85, 0x41300000
	s_lshl_b32 s69, s76, 8
	v_div_scale_f32 v60, s[56:57], s84, s84, v58
	v_rcp_f32_e32 v61, v60
	s_mov_b32 s56, 0xc2fc0000
	v_readlane_b32 s70, v254, 38
	v_readlane_b32 s71, v254, 39
	v_fma_f32 v62, -v60, v61, 1.0
	v_fmac_f32_e32 v61, v62, v61
	v_div_scale_f32 v62, vcc, v58, s84, v58
	v_mul_f32_e32 v63, v62, v61
	v_fma_f32 v64, -v60, v63, v62
	v_fmac_f32_e32 v63, v64, v61
	v_fma_f32 v60, -v60, v63, v62
	v_div_fmas_f32 v60, v60, v61, v63
	v_div_fixup_f32 v58, v60, s84, v58
	v_cmp_gt_f32_e32 vcc, s56, v58
	s_and_b64 s[56:57], vcc, exec
	v_readlane_b32 s56, v254, 48
	s_cselect_b32 s81, 0xffffffc0, 0
	s_add_i32 s56, s69, s56
; #define ATT_WAIT_BAR(N) asm volatile("s_waitcnt vmcnt(" #N ") lgkmcnt(0)\n\ts_barrier" ::: "memory")
; #define ATT_DMA(t, slot) do { glds16(ksrc + (long)(t) * tstep, (unsigned)__builtin_amdgcn_readfirstlane(kdst + (slot))); glds16(vsrc + (long)(t) * tstep, (unsigned)__builtin_amdgcn_readfirstlane(vdst + (slot))); } while (0)
; template <class BIAS>
; __device__ __forceinline__ void attn_tiles(char* shm, const UnitIO& io, int t_begin, int t_end, const BIAS& B, int tid) {
;     ...
;     ATT_DMA(t_begin, 0);
;     asm volatile("" :: "v"(qr[0]), "v"(qr[1]), "v"(qr[2]), "v"(qr[3]));
;     const int nt_ = t_end - t_begin; if (nt_ > 1) ATT_DMA(t_begin + 1, SLOTB); if (nt_ > 2) ATT_DMA(t_begin + 2, 2 * SLOTB);
;     f32x16 o[2]; o[0] = f32x16{}; o[1] = f32x16{}; float l_reg = 0.f;
;     if (nt_ > 2) ATT_WAIT_BAR(4); else if (nt_ > 1) ATT_WAIT_BAR(2); else ATT_WAIT_BAR(0);
; __device__ __forceinline__ void dil_unit(Frame& F, const AttnBufs& A, int b, int h, int g, int r, int c) {
;     ...
;     att::BiasDil B; B.sd = exp2f(-8.0f * (float)(h - 10 + 1) / 10.0f) * LOG2E * (float)dil; B.qrel = 128 + w * 32 + r32; B.hi = hi; B.w = w; B.setup(r32);
;     const long tok_q0 = (long)b * SEQ + r + (long)dil * (i0 + w * 32);
;     const long tok_k0 = (long)b * SEQ + r + (long)dil * (i0 - 128);
;     const long bo = (long)b * (long)BADJ;
;     att::UnitIO io; io.Q = A.Q + bo + tok_q0 * DM + h * 64; io.qstride = (long)DM * dil; io.K0 = A.K + bo + tok_k0 * DM + h * 64; io.V0 = A.V + bo + tok_k0 * DM + h * 64; io.kstride = (long)DM * dil;
;     io.O = A.OD + (size_t)g * OD_BRANCH + tok_q0 * 384 + (h - 10) * 64; io.ostride = (long)384 * dil; io.L = A.LD + (size_t)g * LD_BRANCH + tok_q0 * 8 + (h - 10); io.lstride = (long)8 * dil; io.norm = false;
;     ...
;     att::attn_tiles(shm, io, 5, 6, B, tid);
;     ...
;     att::attn_tiles(shm, io, c == 0 ? 2 : 0, 6, B, tid);
	s_or_b32 s68, s70, s68
	s_ashr_i32 s57, s56, 31
	s_and_b64 s[66:67], s[64:65], exec
	s_cselect_b32 s70, 2, 4
	s_and_b64 s[66:67], s[62:63], exec
	s_cselect_b32 s70, 0, s70
	s_lshl_b64 s[56:57], s[56:57], s70
	s_add_u32 s66, s56, s68
	s_addc_u32 s67, s57, s71
	s_add_i32 s56, s69, 0xffffff80
	s_ashr_i32 s57, s56, 31
	s_lshl_b64 s[56:57], s[56:57], s70
	s_add_u32 s56, s56, s68
	s_addc_u32 s57, s57, s71
	s_lshl_b64 s[68:69], s[66:67], 11
	v_readlane_b32 s70, v254, 42
	s_add_u32 s68, s70, s68
	v_readlane_b32 s70, v254, 45
	s_addc_u32 s69, s70, s69
	s_lshl_b32 s70, s75, 6
	s_lshl_b32 s77, s75, 7
	v_writelane_b32 v255, s70, 49
	v_writelane_b32 v191, s70, 9
	s_add_u32 s70, s68, s77
	s_addc_u32 s71, s69, 0
	s_lshl_b64 s[68:69], s[56:57], 11
	v_readlane_b32 s56, v254, 49
	s_add_u32 s56, s56, s68
	v_readlane_b32 s57, v254, 50
	s_addc_u32 s57, s57, s69
	s_add_u32 s56, s56, s77
	s_addc_u32 s57, s57, 0
	v_readlane_b32 s78, v254, 53
	s_add_u32 s68, s78, s68
	v_readlane_b32 s78, v254, 54
	s_addc_u32 s69, s78, s69
	s_add_u32 s68, s68, s77
	s_addc_u32 s69, s69, 0
	s_cmp_eq_u32 s76, 0
	v_readfirstlane_b32 s77, v232
	s_cselect_b32 s88, 2, 0
	s_ashr_i32 s76, s77, 6
	s_and_b64 s[78:79], s[64:65], exec
	s_cselect_b32 s82, 12, 14
	s_and_b64 s[78:79], s[62:63], exec
	s_cselect_b32 s83, 10, s82
	v_lshlrev_b64 v[60:61], s83, v[146:147]
	v_lshl_add_u64 v[60:61], v[60:61], 1, s[70:71]
	v_mov_b32_e32 v149, v1
	v_lshl_add_u64 v[60:61], v[60:61], 0, v[148:149]
	flat_load_dwordx4 v[98:101], v[60:61] offset:1280
	flat_load_dwordx4 v[102:105], v[60:61] offset:1312
	flat_load_dwordx4 v[106:109], v[60:61] offset:1344
	flat_load_dwordx4 v[110:113], v[60:61] offset:1376
	v_cndmask_b32_e32 v62, 0, v224, vcc
	v_add_f32_e32 v58, v58, v62
	v_exp_f32_e32 v58, v58
	v_cvt_f32_ubyte0_e32 v61, s80
	s_mov_b32 s78, 2.0
	s_mov_b32 s79, 0x40400000
	v_ldexp_f32 v58, v58, s81
	v_mul_f32_e32 v58, 0x3fb8aa3b, v58
	v_mul_f32_e32 v155, v58, v61
	v_mov_b32_e32 v58, v155
	v_pk_mul_f32 v[158:159], v[58:59], s[78:79] op_sel_hi:[0,1]
	s_mov_b32 s78, 0x41000000
	s_mov_b32 s79, 0x41100000
	v_pk_mul_f32 v[160:161], v[58:59], s[78:79] op_sel_hi:[0,1]
	s_mov_b32 s78, 0x41800000
	s_mov_b32 s79, 0x41880000
	v_pk_mul_f32 v[164:165], v[58:59], s[78:79] op_sel_hi:[0,1]
	s_mov_b32 s78, 0x41900000
	s_mov_b32 s79, 0x41980000
	v_pk_mul_f32 v[166:167], v[58:59], s[78:79] op_sel_hi:[0,1]
	s_mov_b32 s78, 0x41c00000
	s_mov_b32 s79, 0x41c80000
	v_pk_mul_f32 v[168:169], v[58:59], s[78:79] op_sel_hi:[0,1]
	s_mov_b32 s78, 0x41d00000
	s_mov_b32 s79, 0x41d80000
	v_pk_mul_f32 v[170:171], v[58:59], s[78:79] op_sel_hi:[0,1]
	s_lshl_b32 s70, s76, 4
	s_ashr_i32 s79, s77, 3
	v_pk_mul_f32 v[162:163], v[58:59], s[84:85] op_sel_hi:[0,1]
	s_lshl_b32 s80, s76, 3
	s_lshl_b32 s78, s76, 10
	v_and_or_b32 v58, s70, 48, v178
	s_and_b32 s82, s79, 0xffffffe0
	v_lshlrev_b64 v[62:63], s83, v[194:195]
	s_ashr_i32 s81, s80, 31
	s_add_i32 s79, s78, 0x8000
	v_lshlrev_b64 v[64:65], s83, v[58:59]
	s_ashr_i32 s83, s82, 31
	v_lshl_add_u64 v[62:63], v[62:63], 1, s[56:57]
	s_and_b64 s[56:57], s[64:65], exec
	v_lshl_add_u64 v[172:173], s[80:81], 1, v[62:63]
	v_lshlrev_b32_e32 v248, 11, v246
	v_mov_b32_e32 v249, s2
	v_lshlrev_b32_e32 v249, 1, v249
	v_lshlrev_b32_e32 v248, v249, v248
	v_add_u32_e32 v248, v248, v247
	v_ashrrev_i32_e32 v249, 31, v248
	v_lshl_add_u64 v[172:173], v[172:173], 0, v[248:249]
	v_lshl_add_u64 v[62:63], v[64:65], 1, s[68:69]
	s_cselect_b32 s68, 18, 20
	s_and_b64 s[56:57], s[62:63], exec
	s_mov_b32 s89, s3
	s_cselect_b32 s80, 16, s68
	v_mov_b32_e32 v66, v150
	v_mov_b32_e32 v67, v1
	v_lshl_add_u64 v[62:63], s[82:83], 1, v[62:63]
	v_lshl_add_u64 v[174:175], v[62:63], 0, v[66:67]
	v_writelane_b32 v254, s2, 9
	v_writelane_b32 v191, s2, 7
	v_writelane_b32 v191, s3, 8
	s_mov_b32 s81, s88
	s_mov_b32 s100, s88
	v_writelane_b32 v191, s62, 0
	v_writelane_b32 v191, s63, 1
	v_writelane_b32 v191, s64, 2
	v_writelane_b32 v191, s65, 3
	v_writelane_b32 v191, s66, 4
	v_writelane_b32 v191, s67, 5
	v_writelane_b32 v191, s75, 6
	s_barrier
.Ldl_pro:
	s_mov_b32 s101, 0
	s_lshl_b64 s[56:57], s[100:101], s80
	s_lshl_b64 s[56:57], s[56:57], 1
	s_add_u32 s56, s56, 0x500
	s_addc_u32 s57, s57, 0
	v_lshl_add_u64 v[62:63], v[172:173], 0, s[56:57]
	v_lshl_add_u64 v[64:65], v[174:175], 0, s[56:57]
	s_lshl_b32 s68, s100, 13
	s_cmp_gt_u32 s100, 3
	s_cselect_b32 s69, 0x14000, 0
	s_add_i32 s68, s68, s69
	s_add_i32 s69, s68, s78
	s_mov_b32 m0, s69
	s_add_i32 s68, s68, s79
	global_load_lds_dwordx4 v[62:63], off
	s_mov_b32 m0, s68
	s_nop 0
	global_load_lds_dwordx4 v[64:65], off
	s_add_i32 s100, s100, 1
	s_cmp_lt_u32 s100, 6
	s_cbranch_scc1 .Ldl_pro
	s_mov_b32 s88, s73
	s_cmp_eq_u32 s74, 0
	s_cbranch_scc1 .Ldl_post
	v_readlane_b32 s62, v190, 0
	v_readlane_b32 s63, v190, 1
	v_readlane_b32 s64, v190, 2
	v_readlane_b32 s65, v190, 3
	v_readlane_b32 s66, v190, 4
	v_readlane_b32 s67, v190, 5
	v_readlane_b32 s75, v190, 6
	s_mov_b32 s100, 0
	s_branch .LBB0_389
.Ldl_ret:
	v_readlane_b32 s62, v191, 0
	v_readlane_b32 s63, v191, 1
	v_readlane_b32 s64, v191, 2
	v_readlane_b32 s65, v191, 3
	v_readlane_b32 s66, v191, 4
	v_readlane_b32 s67, v191, 5
	v_readlane_b32 s75, v191, 6
.Ldl_post:
	v_mov_b32_e32 v190, v191
	v_mov_b32_e32 v2, 0
	s_waitcnt vmcnt(0) lgkmcnt(0)
	s_barrier
	v_mov_b32_e32 v16, v2
	v_mov_b32_e32 v17, v2
	v_mul_f32_e32 v156, 0x42000000, v155
	v_mov_b32_e32 v3, v2
	v_mov_b32_e32 v4, v2
	v_mov_b32_e32 v5, v2
	v_mov_b32_e32 v6, v2
	v_mov_b32_e32 v7, v2
	v_mov_b32_e32 v8, v2
	v_mov_b32_e32 v9, v2
	v_mov_b32_e32 v10, v2
	v_mov_b32_e32 v11, v2
	v_mov_b32_e32 v12, v2
	v_mov_b32_e32 v13, v2
	v_mov_b32_e32 v14, v2
	v_mov_b32_e32 v15, v2
	v_mov_b64_e32 v[32:33], v[16:17]
	v_mul_f32_e32 v149, 0x42800000, v155
	v_mul_f32_e32 v154, 0, v155
	v_writelane_b32 v254, s3, 10
	v_mul_f32_e32 v0, v155, v196
	v_mov_b32_e32 v176, v156
	v_mov_b32_e32 v177, v156
	v_mov_b64_e32 v[30:31], v[14:15]
	v_mov_b64_e32 v[28:29], v[12:13]
	v_mov_b64_e32 v[26:27], v[10:11]
	v_mov_b64_e32 v[24:25], v[8:9]
	v_mov_b64_e32 v[22:23], v[6:7]
	v_mov_b64_e32 v[20:21], v[4:5]
	v_mov_b64_e32 v[18:19], v[2:3]
	v_mov_b32_e32 v151, v2
	s_branch .LBB0_365

; __device__ __forceinline__ int crow(int r, int hi) { return (r & 3) + 8 * (r >> 2) + 4 * hi; }
; template <class BIAS>
; __device__ __forceinline__ void attn_tiles(char* shm, const UnitIO& io, int t_begin, int t_end, const BIAS& B, int tid) {
;     ...
;     { auto rr = __builtin_amdgcn_permlane32_swap(__float_as_uint(l_reg), __float_as_uint(l_reg), false, false); l_reg = __uint_as_float(rr[0]) + __uint_as_float(rr[1]); }
;     if (hi == 0) wsf[32 + r32] = l_reg;
;     asm volatile("s_waitcnt lgkmcnt(0)" ::: "memory");
;     float rli[16];
; #pragma unroll
;     for (int r = 0; r < 16; ++r) rli[r] = io.norm ? __builtin_amdgcn_rcpf(wsf[32 + crow(r, hi)]) : 1.0f;
;     if (!io.norm && hi == 0) io.L[(long)r32 * io.lstride] = l_reg;
.Ldl_unit_done:
	v_readlane_b32 s3, v254, 10
	s_add_i32 s74, s74, 1
	s_cmp_eq_u32 s74, 9
	s_cbranch_scc0 .LBB0_363
	s_mov_b32 s100, 1
.LBB0_389:
	v_mov_b32_e32 v0, v151
	s_nop 1
	v_permlane32_swap_b32_e32 v151, v0
	v_readlane_b32 s2, v255, 3
	v_add_f32_e32 v34, v151, v0
	v_readlane_b32 s3, v255, 4
	s_and_saveexec_b64 s[56:57], s[2:3]
	s_and_b32 s68, s77, 0x3fffffc0
	v_lshl_or_b32 v0, s68, 2, v197
	v_add_u32_e32 v0, 0x10080, v0
	ds_write_b32 v0, v34
	s_or_b64 exec, exec, s[56:57]
	s_waitcnt lgkmcnt(0)
	v_readlane_b32 s2, v255, 3
	v_readlane_b32 s3, v255, 4
	s_and_saveexec_b64 s[56:57], s[2:3]
	s_cbranch_execz .LBB0_362
	v_readlane_b32 s2, v190, 7
	v_readlane_b32 s3, v190, 8
	s_lshl_b64 s[68:69], s[66:67], 5
	s_lshl_b64 s[70:71], s[2:3], 20
	v_readlane_b32 s2, v255, 21
	s_add_u32 s70, s2, s70
	v_readlane_b32 s2, v255, 22
	s_addc_u32 s71, s2, s71
	s_add_u32 s68, s70, s68
	s_addc_u32 s69, s71, s69
	s_lshl_b32 s70, s75, 2
	s_add_u32 s68, s68, s70
	s_addc_u32 s69, s69, 0
	s_and_b64 s[70:71], s[64:65], exec
	s_cselect_b32 s75, 5, 7
	s_and_b64 s[70:71], s[62:63], exec
	s_cselect_b32 s70, 3, s75
	v_lshlrev_b32_e32 v0, s70, v146
	v_lshlrev_b32_e32 v0, 2, v0
	v_lshl_add_u64 v[36:37], s[68:69], 0, v[0:1]
	flat_store_dword v[36:37], v34
	s_branch .LBB0_362
